# tconv8 prologue: the 32 per-tap conditional scalar loads replaced by four 16-byte vector loads per thread (forward or reversed order by wave) plus register moves
# speedup vs baseline: 1.0290x; 1.0046x over previous
.LBB0_438:
	s_add_i32 s38, s36, s30
	s_ashr_i32 s39, s38, 31
	s_lshl_b64 s[4:5], s[38:39], 14
	s_add_u32 s4, s44, s4
	s_addc_u32 s5, s45, s5
	s_addk_i32 s38, 0x600
	s_ashr_i32 s39, s38, 31
	s_lshl_b64 s[38:39], s[38:39], 14
	s_add_u32 s38, s44, s38
	v_mov_b32_e32 v1, v200
	s_movk_i32 s37, 0xff
	s_waitcnt vmcnt(0)
	s_barrier
	s_addc_u32 s39, s45, s39
	s_nop 0
	v_lshlrev_b32_e32 v0, 4, v1
	v_readfirstlane_b32 s98, v1
	s_nop 0
	s_cmp_gt_u32 s98, 0xff
	s_cbranch_scc1 .Lt8_tap_hb
	v_sub_u32_e32 v244, 0xff0, v0
	v_lshl_add_u64 v[2:3], v[244:245], 2, s[4:5]
	s_branch .Lt8_tap_ld
.Lt8_tap_hb:
	v_mov_b32_e32 v1, v245
	v_lshl_add_u64 v[2:3], v[0:1], 2, s[38:39]
	v_add_co_u32_e32 v2, vcc, 0xffffc004, v2
	s_nop 1
	v_addc_co_u32_e32 v3, vcc, -1, v3, vcc
.Lt8_tap_ld:
	global_load_dwordx4 v[20:23], v[2:3], off
	global_load_dwordx4 v[24:27], v[2:3], off offset:16
	global_load_dwordx4 v[28:31], v[2:3], off offset:32
	global_load_dwordx4 v[32:35], v[2:3], off offset:48
	s_ashr_i32 s37, s36, 31
	v_lshl_add_u64 v[18:19], s[36:37], 2, v[176:177]
	global_load_dword v17, v[18:19], off
	s_waitcnt vmcnt(1)
	s_cmp_gt_u32 s98, 0xff
	s_cbranch_scc1 .Lt8_mov_hb
	v_mov_b32_e32 v2, v35
	v_mov_b32_e32 v3, v34
	v_mov_b32_e32 v4, v33
	v_mov_b32_e32 v5, v32
	v_mov_b32_e32 v6, v31
	v_mov_b32_e32 v7, v30
	v_mov_b32_e32 v8, v29
	v_mov_b32_e32 v9, v28
	v_mov_b32_e32 v10, v27
	v_mov_b32_e32 v11, v26
	v_mov_b32_e32 v12, v25
	v_mov_b32_e32 v13, v24
	v_mov_b32_e32 v14, v23
	v_mov_b32_e32 v15, v22
	v_mov_b32_e32 v16, v21
	v_mov_b32_e32 v1, v20
	s_branch .Lt8_mov_done
.Lt8_mov_hb:
	v_mov_b32_e32 v2, v20
	v_mov_b32_e32 v3, v21
	v_mov_b32_e32 v4, v22
	v_mov_b32_e32 v5, v23
	v_mov_b32_e32 v6, v24
	v_mov_b32_e32 v7, v25
	v_mov_b32_e32 v8, v26
	v_mov_b32_e32 v9, v27
	v_mov_b32_e32 v10, v28
	v_mov_b32_e32 v11, v29
	v_mov_b32_e32 v12, v30
	v_mov_b32_e32 v13, v31
	v_mov_b32_e32 v14, v32
	v_mov_b32_e32 v15, v33
	v_mov_b32_e32 v16, v34
	v_cmp_eq_u32_e32 vcc, 0x1ff, v200
	s_nop 1
	v_cndmask_b32_e32 v1, v35, v245, vcc
.Lt8_mov_done:
	v_max3_f32 v0, |v2|, 0, |v3|
	v_max3_f32 v0, v0, |v4|, |v5|
	v_max3_f32 v0, v0, |v6|, |v7|
	v_mov_b32_e32 v18, v245
	v_max3_f32 v0, v0, |v8|, |v9|
	v_max3_f32 v0, v0, |v10|, |v11|
	v_max3_f32 v0, v0, |v12|, |v13|
	v_max3_f32 v0, v0, |v14|, |v15|
	v_max3_f32 v0, v0, |v16|, |v1|
	s_waitcnt vmcnt(0)
	v_add_f32_dpp v17, v17, v17 quad_perm:[1,0,3,2] row_mask:0xf bank_mask:0xf bound_ctrl:1
	s_nop 1
	v_add_f32_dpp v17, v17, v17 quad_perm:[2,3,0,1] row_mask:0xf bank_mask:0xf bound_ctrl:1
	s_nop 1
	v_add_f32_dpp v17, v17, v17 row_half_mirror row_mask:0xf bank_mask:0xf bound_ctrl:1
	s_nop 1
	v_add_f32_dpp v17, v17, v17 row_mirror row_mask:0xf bank_mask:0xf bound_ctrl:1
	s_nop 1
	v_mov_b32_dpp v18, v17 row_bcast:15 row_mask:0xa bank_mask:0xf
	v_add_f32_e32 v17, v17, v18
	v_mov_b32_e32 v18, v245
	s_nop 1
	v_mov_b32_dpp v18, v17 row_bcast:31 row_mask:0xc bank_mask:0xf
	v_add_f32_e32 v17, v17, v18
	s_nop 0
	v_readlane_b32 s38, v17, 63
	v_mov_b32_e32 v17, v245
	s_nop 1
	v_mov_b32_dpp v17, v0 quad_perm:[1,0,3,2] row_mask:0xf bank_mask:0xf
	v_max_f32_e32 v17, v17, v17
	v_max_f32_e32 v0, v0, v17
	v_mov_b32_e32 v17, v245
	s_nop 1
	v_mov_b32_dpp v17, v0 quad_perm:[2,3,0,1] row_mask:0xf bank_mask:0xf
	v_max_f32_e32 v17, v17, v17
	v_max_f32_e32 v0, v0, v17
	v_mov_b32_e32 v17, v245
	s_nop 1
	v_mov_b32_dpp v17, v0 row_half_mirror row_mask:0xf bank_mask:0xf
	v_max_f32_e32 v17, v17, v17
	v_max_f32_e32 v0, v0, v17
	v_mov_b32_e32 v17, v245
	s_nop 1
	v_mov_b32_dpp v17, v0 row_mirror row_mask:0xf bank_mask:0xf
	v_max_f32_e32 v17, v17, v17
	v_max_f32_e32 v0, v0, v17
	v_mov_b32_e32 v17, v245
	s_nop 1
	v_mov_b32_dpp v17, v0 row_bcast:15 row_mask:0xa bank_mask:0xf
	v_max_f32_e32 v17, v17, v17
	v_max_f32_e32 v0, v0, v17
	v_mov_b32_e32 v17, v245
	s_nop 1
	v_mov_b32_dpp v17, v0 row_bcast:31 row_mask:0xc bank_mask:0xf
	v_max_f32_e32 v17, v17, v17
	v_max_f32_e32 v0, v0, v17
	s_nop 0
	v_readlane_b32 s39, v0, 63
	s_and_saveexec_b64 s[4:5], s[0:1]
	v_mov_b32_e32 v0, s47
	v_mov_b32_e32 v17, s38
	v_mov_b32_e32 v18, s39
	ds_write2_b32 v0, v17, v18 offset1:8
	s_or_b64 exec, exec, s[4:5]
	s_add_i32 s4, 0, 0x21000
	v_mov_b32_e32 v0, s4
	s_waitcnt lgkmcnt(0)
	s_barrier
	ds_read_b128 v[18:21], v0
	v_readlane_b32 s4, v254, 49
	v_mov_b32_e32 v40, 0
	s_nop 0
	v_mov_b32_e32 v17, s4
	ds_read_b128 v[22:25], v17
	s_waitcnt lgkmcnt(1)
	v_add_f32_e32 v0, 0, v18
	v_add_f32_e32 v0, v0, v19
	v_readlane_b32 s4, v254, 50
	v_add_f32_e32 v0, v0, v20
	v_add_f32_e32 v0, v0, v21
	v_mov_b32_e32 v18, s4
	ds_read_b128 v[18:21], v18
	v_readlane_b32 s4, v254, 51
	s_waitcnt lgkmcnt(1)
	v_max3_f32 v17, v22, 0, v23
	v_max3_f32 v17, v17, v24, v25
	s_waitcnt lgkmcnt(0)
	v_add_f32_e32 v0, v0, v18
	v_add_f32_e32 v0, v0, v19
	v_add_f32_e32 v0, v0, v20
	v_mov_b32_e32 v18, s4
	v_add_f32_e32 v0, v0, v21
	ds_read_b128 v[22:25], v18
	v_div_scale_f32 v18, s[4:5], v0, v0, 1.0
	v_rcp_f32_e32 v19, v18
	s_waitcnt lgkmcnt(0)
	v_max3_f32 v17, v17, v22, v23
	v_max3_f32 v17, v17, v24, v25
	v_fma_f32 v20, -v18, v19, 1.0
	v_fmac_f32_e32 v19, v20, v19
	v_div_scale_f32 v20, vcc, 1.0, v0, 1.0
	v_mul_f32_e32 v21, v20, v19
	v_fma_f32 v22, -v18, v21, v20
	v_fmac_f32_e32 v21, v22, v19
	v_fma_f32 v18, -v18, v21, v20
	v_div_fmas_f32 v18, v18, v19, v21
	v_div_fixup_f32 v0, v18, v0, 1.0
	v_mul_f32_e32 v17, v17, v0
	v_max_f32_e32 v17, 0xda24260, v17
	v_frexp_exp_i32_f32_e32 v17, v17
	v_sub_u32_e32 v18, 7, v17
	v_ldexp_f32 v18, 1.0, v18
	v_mul_f32_e32 v0, v0, v18
	v_mul_f32_e32 v18, v2, v0
	v_mul_f32_e32 v3, v3, v0
	v_mov_b32_e32 v2, 0
	v_cvt_pk_fp8_f32 v2, v18, v3
	v_mul_f32_e32 v3, v4, v0
	v_mul_f32_e32 v4, v5, v0
	v_mul_f32_e32 v5, v7, v0
	v_cvt_pk_fp8_f32 v2, v3, v4 op_sel:[0,0,1]
	v_mul_f32_e32 v4, v6, v0
	v_mov_b32_e32 v3, 0
	v_cvt_pk_fp8_f32 v3, v4, v5
	v_mul_f32_e32 v4, v8, v0
	v_mul_f32_e32 v5, v9, v0
	v_mul_f32_e32 v6, v11, v0
	v_cvt_pk_fp8_f32 v3, v4, v5 op_sel:[0,0,1]
	v_mul_f32_e32 v5, v10, v0
	v_mov_b32_e32 v4, 0
	v_cvt_pk_fp8_f32 v4, v5, v6
	v_mul_f32_e32 v5, v12, v0
	v_mul_f32_e32 v6, v13, v0
	v_mul_f32_e32 v7, v15, v0
	v_cvt_pk_fp8_f32 v4, v5, v6 op_sel:[0,0,1]
	v_mul_f32_e32 v6, v14, v0
	v_mov_b32_e32 v5, 0
	v_cvt_pk_fp8_f32 v5, v6, v7
	v_mul_f32_e32 v6, v16, v0
	v_mul_f32_e32 v0, v1, v0
	v_mov_b32_e32 v7, 0
	v_cvt_pk_fp8_f32 v5, v6, v0 op_sel:[0,0,1]
	v_mov_b32_e32 v6, 0
	ds_write_b128 v193, v[2:5]
	s_waitcnt lgkmcnt(0)
	s_barrier
	ds_read_b128 v[8:11], v193
	v_mov_b32_e32 v2, 0
	v_mov_b32_e32 v3, 0
	s_and_saveexec_b64 s[4:5], s[6:7]
	s_cbranch_execz .LBB0_538
	ds_read_b128 v[0:3], v193 offset:16
	s_waitcnt lgkmcnt(0)
	v_mov_b32_e32 v6, v0
	v_mov_b32_e32 v7, v1
